# LN2 loop software-pipelined: next iteration's token (expert, slot) words prefetched at the top of the current iteration; later iterations start without draining the previous stores
# baseline (speedup 1.0000x reference)
; __global__ void __launch_bounds__(NTHREADS, 2) hybrid_fwd(Args a) {
;     ...
;             for (int row0 = gw; row0 < MTOK; row0 += 2 * NGW) {
;                 int sl[2][2];
; #pragma unroll
;                 for (int rr = 0; rr < 2; ++rr) { const int row = row0 + rr * NGW; sl[rr][0] = meta[16 + tokE[row * 2]] + tokS[row * 2]; sl[rr][1] = meta[16 + tokE[row * 2 + 1]] + tokS[row * 2 + 1]; }
;                 u32x2 xw[2][8]; unsigned pw_[2][8], qw[2][8];
; #pragma unroll
;                 for (int rr = 0; rr < 2; ++rr) { const int row = row0 + rr * NGW;
; #pragma unroll
;                     for (int j = 0; j < 8; ++j) { xw[rr][j] = __builtin_nontemporal_load((const u32x2*)(X1B + (size_t)row * DM + j * 256 + lane * 4));
;                         pw_[rr][j] = __builtin_nontemporal_load((const unsigned*)(Y2 + (size_t)sl[rr][0] * DM + j * 256 + lane * 4)); qw[rr][j] = __builtin_nontemporal_load((const unsigned*)(Y2 + (size_t)sl[rr][1] * DM + j * 256 + lane * 4)); } }
.LBB0_1336:
	s_mov_b32 s22, s27
	s_mov_b32 s23, s30
	s_mov_b32 s34, s25
	s_mov_b32 s35, s26
	s_cmp_lt_u32 s12, s36
	s_cbranch_scc0 .Lpf_have
	s_lshl_b32 s2, s18, 2
	s_add_i32 s3, s36, s18
	s_lshl_b32 s3, s3, 2
	v_mov_b32_e32 v6, s2
	v_mov_b32_e32 v7, s3
	global_load_dwordx2 v[132:133], v6, s[22:23]
	global_load_dwordx2 v[134:135], v6, s[34:35]
	global_load_dwordx2 v[136:137], v7, s[22:23]
	global_load_dwordx2 v[138:139], v7, s[34:35]
	s_waitcnt vmcnt(0)
.Lpf_have:
	v_mov_b32_e32 v0, v132
	v_mov_b32_e32 v1, v133
	v_mov_b32_e32 v2, v134
	v_mov_b32_e32 v3, v135
	v_mov_b32_e32 v4, v136
	v_mov_b32_e32 v5, v137
	v_mov_b32_e32 v46, v138
	v_mov_b32_e32 v47, v139
	s_add_i32 s2, s12, s36
	s_cmpk_gt_i32 s2, 0x1fff
	s_cbranch_scc1 .Lpf_none
	s_add_i32 s2, s18, s94
	s_add_i32 s3, s36, s2
	s_lshl_b32 s2, s2, 2
	s_lshl_b32 s3, s3, 2
	v_mov_b32_e32 v6, s2
	v_mov_b32_e32 v7, s3
	global_load_dwordx2 v[132:133], v6, s[22:23]
	global_load_dwordx2 v[134:135], v6, s[34:35]
	global_load_dwordx2 v[136:137], v7, s[22:23]
	global_load_dwordx2 v[138:139], v7, s[34:35]
.Lpf_none:
	v_lshl_add_u64 v[40:41], s[4:5], 0, v[32:33]
	v_lshl_add_u32 v0, v0, 2, s31
	v_lshl_add_u32 v1, v1, 2, s31
	v_lshl_add_u32 v4, v4, 2, s31
	v_lshl_add_u32 v5, v5, 2, s31
	ds_read_b32 v0, v0 offset:64
	ds_read_b32 v1, v1 offset:64
	ds_read_b32 v4, v4 offset:64
	ds_read_b32 v5, v5 offset:64
	s_waitcnt lgkmcnt(0)
	v_add_u32_e32 v0, v2, v0
	v_add_u32_e32 v2, v3, v1
	v_add_u32_e32 v42, v46, v4
	v_add_u32_e32 v44, v47, v5
	s_mov_b32 s2, 0x42000000
	v_ashrrev_i32_e32 v43, 31, v42
	v_lshlrev_b64 v[42:43], 11, v[42:43]
	v_lshl_add_u64 v[70:71], v[8:9], 0, v[42:43]
	v_ashrrev_i32_e32 v1, 31, v0
	v_lshlrev_b64 v[0:1], 11, v[0:1]
	v_ashrrev_i32_e32 v3, 31, v2
	v_lshl_add_u64 v[38:39], v[8:9], 0, v[0:1]
	v_lshlrev_b64 v[0:1], 11, v[2:3]
	v_lshl_add_u64 v[46:47], v[8:9], 0, v[0:1]
	v_add_co_u32_e32 v0, vcc, s2, v40
	v_ashrrev_i32_e32 v45, 31, v44
	s_nop 0
	v_addc_co_u32_e32 v1, vcc, 0, v41, vcc
	flat_load_dwordx2 v[64:65], v[0:1] nt
	flat_load_dword v74, v[38:39] nt
	flat_load_dword v76, v[46:47] nt
	flat_load_dwordx2 v[62:63], v[0:1] offset:512 nt
	flat_load_dword v80, v[38:39] offset:256 nt
	flat_load_dword v81, v[46:47] offset:256 nt
	flat_load_dwordx2 v[60:61], v[0:1] offset:1024 nt
	flat_load_dword v90, v[38:39] offset:512 nt
	flat_load_dword v91, v[46:47] offset:512 nt
	flat_load_dwordx2 v[58:59], v[0:1] offset:1536 nt
	flat_load_dword v110, v[38:39] offset:768 nt
	flat_load_dword v111, v[46:47] offset:768 nt
	flat_load_dwordx2 v[6:7], v[0:1] offset:2048 nt
	flat_load_dword v69, v[38:39] offset:1024 nt
	flat_load_dword v68, v[46:47] offset:1024 nt
	flat_load_dwordx2 v[4:5], v[0:1] offset:2560 nt
	flat_load_dword v67, v[38:39] offset:1280 nt
	flat_load_dword v66, v[46:47] offset:1280 nt
	flat_load_dwordx2 v[2:3], v[0:1] offset:3072 nt
	flat_load_dword v89, v[38:39] offset:1536 nt
	flat_load_dword v88, v[46:47] offset:1536 nt
	s_nop 0
	flat_load_dwordx2 v[0:1], v[0:1] offset:3584 nt
	s_nop 0
	flat_load_dword v87, v[38:39] offset:1792 nt
	flat_load_dword v86, v[46:47] offset:1792 nt
	v_lshl_add_u64 v[38:39], s[4:5], 0, v[36:37]
	v_lshlrev_b64 v[42:43], 11, v[44:45]
	v_lshl_add_u64 v[72:73], v[8:9], 0, v[42:43]
	v_add_co_u32_e32 v42, vcc, s2, v38
	s_mov_b64 s[2:3], -1
	s_nop 0
	v_addc_co_u32_e32 v43, vcc, 0, v39, vcc
	flat_load_dwordx2 v[56:57], v[42:43] nt
	flat_load_dword v109, v[70:71] nt
	flat_load_dword v108, v[72:73] nt
	flat_load_dwordx2 v[52:53], v[42:43] offset:512 nt
	flat_load_dword v106, v[70:71] offset:256 nt
	flat_load_dword v104, v[72:73] offset:256 nt
	flat_load_dwordx2 v[48:49], v[42:43] offset:1024 nt
	flat_load_dword v101, v[70:71] offset:512 nt
	flat_load_dword v100, v[72:73] offset:512 nt
	flat_load_dwordx2 v[54:55], v[42:43] offset:1536 nt
	flat_load_dword v107, v[70:71] offset:768 nt
	flat_load_dword v105, v[72:73] offset:768 nt
	flat_load_dwordx2 v[50:51], v[42:43] offset:2048 nt
	flat_load_dword v103, v[70:71] offset:1024 nt
	flat_load_dword v102, v[72:73] offset:1024 nt
	flat_load_dwordx2 v[46:47], v[42:43] offset:2560 nt
	flat_load_dword v99, v[70:71] offset:1280 nt
	flat_load_dword v98, v[72:73] offset:1280 nt
	flat_load_dwordx2 v[44:45], v[42:43] offset:3072 nt
	flat_load_dword v97, v[70:71] offset:1536 nt
	flat_load_dword v96, v[72:73] offset:1536 nt
	s_nop 0
	flat_load_dwordx2 v[42:43], v[42:43] offset:3584 nt
	s_nop 0
	flat_load_dword v95, v[70:71] offset:1792 nt
	flat_load_dword v94, v[72:73] offset:1792 nt
	s_and_b64 vcc, exec, s[14:15]
	s_waitcnt vmcnt(0) lgkmcnt(0)
; __device__ __forceinline__ float bflo(unsigned w) { return __uint_as_float(w << 16); }
; __device__ __forceinline__ float bfhi(unsigned w) { return __uint_as_float(w & 0xffff0000u); }
; __global__ void __launch_bounds__(NTHREADS, 2) hybrid_fwd(Args a) {
;     ...
;                 for (int rr = 0; rr < 2; ++rr) { const int row = row0 + rr * NGW;
;                     f32x4 y[8]; float s = 0.f;
; #pragma unroll
;                     for (int j = 0; j < 8; ++j) { const u32x2 x = xw[rr][j]; const int p = (int)pw_[rr][j], q = (int)qw[rr][j];
;                         const f32x2 p0 = __builtin_amdgcn_cvt_pk_f32_fp8(p, false), p1 = __builtin_amdgcn_cvt_pk_f32_fp8(p, true), q0 = __builtin_amdgcn_cvt_pk_f32_fp8(q, false), q1 = __builtin_amdgcn_cvt_pk_f32_fp8(q, true);
;                         y[j][0] = bflo(x.x) * ALPHA + (p0.x + q0.x) * (1.f / Y2_SCALE); y[j][1] = bfhi(x.x) * ALPHA + (p0.y + q0.y) * (1.f / Y2_SCALE);
;                         y[j][2] = bflo(x.y) * ALPHA + (p1.x + q1.x) * (1.f / Y2_SCALE); y[j][3] = bfhi(x.y) * ALPHA + (p1.y + q1.y) * (1.f / Y2_SCALE);
;                         s += (y[j][0] + y[j][1]) + (y[j][2] + y[j][3]); }
	v_lshlrev_b32_e32 v78, 16, v64
	v_cvt_pk_f32_fp8_e32 v[70:71], v74
	v_cvt_pk_f32_fp8_sdwa v[72:73], v74 src0_sel:WORD_1
	v_cvt_pk_f32_fp8_e32 v[74:75], v76
	v_cvt_pk_f32_fp8_sdwa v[76:77], v76 src0_sel:WORD_1
	v_and_b32_e32 v79, 0xffff0000, v64
	v_lshlrev_b32_e32 v64, 16, v65
	v_pk_add_f32 v[70:71], v[70:71], v[74:75]
	v_and_b32_e32 v65, 0xffff0000, v65
	v_pk_mul_f32 v[70:71], v[70:71], s[72:73] op_sel_hi:[1,0]
	v_cvt_pk_f32_fp8_sdwa v[74:75], v81 src0_sel:WORD_1
	v_pk_fma_f32 v[82:83], v[78:79], s[90:91], v[70:71] op_sel_hi:[1,0,1]
	v_pk_add_f32 v[70:71], v[72:73], v[76:77]
	v_cvt_pk_f32_fp8_e32 v[72:73], v81
	v_pk_mul_f32 v[70:71], v[70:71], s[72:73] op_sel_hi:[1,0]
	v_lshlrev_b32_e32 v76, 16, v62
	v_pk_fma_f32 v[84:85], v[64:65], s[90:91], v[70:71] op_sel_hi:[1,0,1]
	v_add_f32_e32 v65, v82, v83
	v_add_f32_e32 v64, v85, v84
	v_add_f32_e32 v64, v65, v64
	v_add_f32_e32 v78, 0, v64
	v_cvt_pk_f32_fp8_e32 v[64:65], v80
	v_cvt_pk_f32_fp8_sdwa v[70:71], v80 src0_sel:WORD_1
	v_and_b32_e32 v77, 0xffff0000, v62
	v_lshlrev_b32_e32 v62, 16, v63
	v_pk_add_f32 v[64:65], v[64:65], v[72:73]
	v_pk_add_f32 v[70:71], v[70:71], v[74:75]
	v_pk_mul_f32 v[64:65], v[64:65], s[72:73] op_sel_hi:[1,0]
	v_and_b32_e32 v63, 0xffff0000, v63
	v_pk_mul_f32 v[70:71], v[70:71], s[72:73] op_sel_hi:[1,0]
	v_pk_fma_f32 v[64:65], v[76:77], s[90:91], v[64:65] op_sel_hi:[1,0,1]
	v_pk_fma_f32 v[80:81], v[62:63], s[90:91], v[70:71] op_sel_hi:[1,0,1]
	v_add_f32_e32 v63, v64, v65
	v_add_f32_e32 v62, v81, v80
	v_add_f32_e32 v62, v63, v62
	v_add_f32_e32 v112, v78, v62
	v_cvt_pk_f32_fp8_e32 v[62:63], v90
	v_cvt_pk_f32_fp8_e32 v[72:73], v91
	v_cvt_pk_f32_fp8_sdwa v[70:71], v90 src0_sel:WORD_1
	v_cvt_pk_f32_fp8_sdwa v[74:75], v91 src0_sel:WORD_1
	v_lshlrev_b32_e32 v76, 16, v60
	v_pk_add_f32 v[62:63], v[62:63], v[72:73]
	v_and_b32_e32 v77, 0xffff0000, v60
	v_pk_mul_f32 v[62:63], v[62:63], s[72:73] op_sel_hi:[1,0]
	v_lshlrev_b32_e32 v60, 16, v61
	v_pk_fma_f32 v[72:73], v[76:77], s[90:91], v[62:63] op_sel_hi:[1,0,1]
	v_pk_add_f32 v[62:63], v[70:71], v[74:75]
	v_and_b32_e32 v61, 0xffff0000, v61
	v_pk_mul_f32 v[62:63], v[62:63], s[72:73] op_sel_hi:[1,0]
	v_cvt_pk_f32_fp8_e32 v[70:71], v111
	v_pk_fma_f32 v[78:79], v[60:61], s[90:91], v[62:63] op_sel_hi:[1,0,1]
	v_add_f32_e32 v61, v72, v73
	v_add_f32_e32 v60, v79, v78
	v_add_f32_e32 v60, v61, v60
	v_add_f32_e32 v90, v112, v60
	v_cvt_pk_f32_fp8_e32 v[60:61], v110
	v_cvt_pk_f32_fp8_sdwa v[62:63], v110 src0_sel:WORD_1
	v_cvt_pk_f32_fp8_sdwa v[74:75], v111 src0_sel:WORD_1
	v_lshlrev_b32_e32 v76, 16, v58
	v_pk_add_f32 v[60:61], v[60:61], v[70:71]
	v_and_b32_e32 v77, 0xffff0000, v58
	v_pk_mul_f32 v[60:61], v[60:61], s[72:73] op_sel_hi:[1,0]
	v_lshlrev_b32_e32 v58, 16, v59
	v_pk_fma_f32 v[70:71], v[76:77], s[90:91], v[60:61] op_sel_hi:[1,0,1]
	v_pk_add_f32 v[60:61], v[62:63], v[74:75]
	v_and_b32_e32 v59, 0xffff0000, v59
	v_pk_mul_f32 v[60:61], v[60:61], s[72:73] op_sel_hi:[1,0]
	v_cvt_pk_f32_fp8_e32 v[62:63], v68
	v_pk_fma_f32 v[76:77], v[58:59], s[90:91], v[60:61] op_sel_hi:[1,0,1]
	v_add_f32_e32 v59, v70, v71
	v_add_f32_e32 v58, v77, v76
	v_add_f32_e32 v58, v59, v58
	v_add_f32_e32 v90, v90, v58
	v_cvt_pk_f32_fp8_e32 v[58:59], v69
	v_cvt_pk_f32_fp8_sdwa v[60:61], v69 src0_sel:WORD_1
	v_cvt_pk_f32_fp8_sdwa v[74:75], v68 src0_sel:WORD_1
	v_lshlrev_b32_e32 v68, 16, v6
	v_pk_add_f32 v[58:59], v[58:59], v[62:63]
	v_and_b32_e32 v69, 0xffff0000, v6
	v_pk_mul_f32 v[58:59], v[58:59], s[72:73] op_sel_hi:[1,0]
	v_lshlrev_b32_e32 v6, 16, v7
	v_pk_fma_f32 v[68:69], v[68:69], s[90:91], v[58:59] op_sel_hi:[1,0,1]
	v_pk_add_f32 v[58:59], v[60:61], v[74:75]
	v_and_b32_e32 v7, 0xffff0000, v7
	v_pk_mul_f32 v[58:59], v[58:59], s[72:73] op_sel_hi:[1,0]
	v_cvt_pk_f32_fp8_e32 v[60:61], v66
	v_pk_fma_f32 v[74:75], v[6:7], s[90:91], v[58:59] op_sel_hi:[1,0,1]
	v_add_f32_e32 v7, v68, v69
	v_add_f32_e32 v6, v75, v74
	v_add_f32_e32 v6, v7, v6
	v_add_f32_e32 v90, v90, v6
	v_cvt_pk_f32_fp8_e32 v[6:7], v67
	v_cvt_pk_f32_fp8_sdwa v[58:59], v67 src0_sel:WORD_1
	v_cvt_pk_f32_fp8_sdwa v[66:67], v66 src0_sel:WORD_1
	v_lshlrev_b32_e32 v62, 16, v4
	v_pk_add_f32 v[6:7], v[6:7], v[60:61]
	v_and_b32_e32 v63, 0xffff0000, v4
	v_pk_mul_f32 v[6:7], v[6:7], s[72:73] op_sel_hi:[1,0]
	v_lshlrev_b32_e32 v4, 16, v5
	v_pk_fma_f32 v[62:63], v[62:63], s[90:91], v[6:7] op_sel_hi:[1,0,1]
	v_pk_add_f32 v[6:7], v[58:59], v[66:67]
	v_and_b32_e32 v5, 0xffff0000, v5
	v_pk_mul_f32 v[6:7], v[6:7], s[72:73] op_sel_hi:[1,0]
	v_cvt_pk_f32_fp8_e32 v[58:59], v88
	v_pk_fma_f32 v[66:67], v[4:5], s[90:91], v[6:7] op_sel_hi:[1,0,1]
	v_add_f32_e32 v5, v62, v63
	v_add_f32_e32 v4, v67, v66
	v_add_f32_e32 v4, v5, v4
	v_add_f32_e32 v90, v90, v4
	v_cvt_pk_f32_fp8_e32 v[4:5], v89
	v_cvt_pk_f32_fp8_sdwa v[6:7], v89 src0_sel:WORD_1
	v_cvt_pk_f32_fp8_sdwa v[60:61], v88 src0_sel:WORD_1
	v_lshlrev_b32_e32 v88, 16, v2
	v_pk_add_f32 v[4:5], v[4:5], v[58:59]
	v_and_b32_e32 v89, 0xffff0000, v2
	v_pk_mul_f32 v[4:5], v[4:5], s[72:73] op_sel_hi:[1,0]
	v_lshlrev_b32_e32 v2, 16, v3
	v_pk_fma_f32 v[58:59], v[88:89], s[90:91], v[4:5] op_sel_hi:[1,0,1]
	v_pk_add_f32 v[4:5], v[6:7], v[60:61]
; __device__ __forceinline__ unsigned cvt_pk_bf16(float lo, float hi) { unsigned r; asm volatile("v_cvt_pk_bf16_f32 %0, %1, %2" : "=v"(r) : "v"(lo), "v"(hi)); return r; }
; __global__ void __launch_bounds__(NTHREADS, 2) hybrid_fwd(Args a) {
;     ...
;                         s += (y[j][0] + y[j][1]) + (y[j][2] + y[j][3]); }
;                     const float mean = wave_sum(s) * (1.f / DM); float s2 = 0.f;
; #pragma unroll
;                     for (int j = 0; j < 8; ++j) { y[j] = y[j] - mean; s2 += (y[j][0] * y[j][0] + y[j][1] * y[j][1]) + (y[j][2] * y[j][2] + y[j][3] * y[j][3]); }
;                     const float rstd = __builtin_amdgcn_rsqf(wave_sum(s2) * (1.f / DM) + LN_EPS);
; #pragma unroll
;                     for (int j = 0; j < 8; ++j) { const f32x4 gg = *(const f32x4*)(lg + j * 256 + lane * 4), bb = *(const f32x4*)(lb + j * 256 + lane * 4);
;                         y[j] = y[j] * rstd * gg + bb;
;                         if (lastl) __builtin_nontemporal_store(y[j], (f32x4*)(a.out + (size_t)row * DM + j * 256 + lane * 4));
;                         else { u32x2 w; w.x = cvt_pk_bf16(y[j][0], y[j][1]); w.y = cvt_pk_bf16(y[j][2], y[j][3]); __builtin_nontemporal_store(w, (u32x2*)(XA16 + (size_t)row * DM + j * 256 + lane * 4)); }
;                         if (!lastl) __builtin_nontemporal_store(cvt4_fp8(y[j][0], y[j][1], y[j][2], y[j][3]), (unsigned*)(XB + (size_t)row * DM + j * 256 + lane * 4)); }
	v_and_b32_e32 v3, 0xffff0000, v3
	v_pk_mul_f32 v[4:5], v[4:5], s[72:73] op_sel_hi:[1,0]
	v_cvt_pk_f32_fp8_e32 v[88:89], v86
	v_pk_fma_f32 v[60:61], v[2:3], s[90:91], v[4:5] op_sel_hi:[1,0,1]
	v_add_f32_e32 v3, v58, v59
	v_add_f32_e32 v2, v61, v60
	v_cvt_pk_f32_fp8_e32 v[4:5], v87
	v_add_f32_e32 v2, v3, v2
	v_add_f32_e32 v2, v90, v2
	v_cvt_pk_f32_fp8_sdwa v[6:7], v87 src0_sel:WORD_1
	v_cvt_pk_f32_fp8_sdwa v[90:91], v86 src0_sel:WORD_1
	v_pk_add_f32 v[4:5], v[4:5], v[88:89]
	v_lshlrev_b32_e32 v86, 16, v0
	v_and_b32_e32 v87, 0xffff0000, v0
	v_pk_mul_f32 v[4:5], v[4:5], s[72:73] op_sel_hi:[1,0]
	v_lshlrev_b32_e32 v0, 16, v1
	v_pk_fma_f32 v[86:87], v[86:87], s[90:91], v[4:5] op_sel_hi:[1,0,1]
	v_pk_add_f32 v[4:5], v[6:7], v[90:91]
	v_and_b32_e32 v1, 0xffff0000, v1
	v_pk_mul_f32 v[4:5], v[4:5], s[72:73] op_sel_hi:[1,0]
	s_nop 0
	v_pk_fma_f32 v[88:89], v[0:1], s[90:91], v[4:5] op_sel_hi:[1,0,1]
	v_add_f32_e32 v1, v86, v87
	v_add_f32_e32 v0, v89, v88
	v_add_f32_e32 v0, v1, v0
	v_add_f32_e32 v0, v2, v0
	s_nop 1
	v_add_f32_dpp v0, v0, v0 quad_perm:[1,0,3,2] row_mask:0xf bank_mask:0xf bound_ctrl:1
	s_nop 1
	v_add_f32_dpp v0, v0, v0 quad_perm:[2,3,0,1] row_mask:0xf bank_mask:0xf bound_ctrl:1
	s_nop 1
	v_add_f32_dpp v0, v0, v0 row_ror:4 row_mask:0xf bank_mask:0xf bound_ctrl:1
	s_nop 1
	v_add_f32_dpp v0, v0, v0 row_ror:8 row_mask:0xf bank_mask:0xf bound_ctrl:1
	v_mov_b32_e32 v1, v0
	s_nop 1
	v_permlane16_swap_b32_e32 v0, v1
	v_add_f32_e32 v0, v0, v1
	v_mov_b32_e32 v1, v0
	s_nop 1
	v_permlane32_swap_b32_e32 v0, v1
	v_add_f32_e32 v0, v0, v1
	v_fmac_f32_e32 v85, 0xba000000, v0
	v_fmac_f32_e32 v83, 0xba000000, v0
	v_fmamk_f32 v84, v0, 0xba000000, v84
	v_fmamk_f32 v82, v0, 0xba000000, v82
	v_mul_f32_e32 v1, v83, v83
	v_mul_f32_e32 v2, v85, v85
	v_fmac_f32_e32 v1, v82, v82
	v_fmac_f32_e32 v2, v84, v84
	v_fmamk_f32 v81, v0, 0xba000000, v81
	v_fmamk_f32 v65, v0, 0xba000000, v65
	v_add_f32_e32 v1, v1, v2
	v_fmac_f32_e32 v80, 0xba000000, v0
	v_fmac_f32_e32 v64, 0xba000000, v0
	v_mul_f32_e32 v2, v65, v65
	v_mul_f32_e32 v3, v81, v81
	v_fmac_f32_e32 v2, v64, v64
	v_fmac_f32_e32 v3, v80, v80
	v_add_f32_e32 v2, v2, v3
	v_fmamk_f32 v79, v0, 0xba000000, v79
	v_fmamk_f32 v73, v0, 0xba000000, v73
	v_add_f32_e32 v1, v1, v2
	v_fmac_f32_e32 v78, 0xba000000, v0
	v_fmac_f32_e32 v72, 0xba000000, v0
	v_mul_f32_e32 v2, v73, v73
	v_mul_f32_e32 v3, v79, v79
	v_fmac_f32_e32 v2, v72, v72
	v_fmac_f32_e32 v3, v78, v78
	v_add_f32_e32 v2, v2, v3
	v_fmamk_f32 v77, v0, 0xba000000, v77
	v_fmamk_f32 v71, v0, 0xba000000, v71
	v_add_f32_e32 v1, v1, v2
	v_fmac_f32_e32 v76, 0xba000000, v0
	v_fmac_f32_e32 v70, 0xba000000, v0
	v_mul_f32_e32 v2, v71, v71
	v_mul_f32_e32 v3, v77, v77
	v_fmac_f32_e32 v2, v70, v70
	v_fmac_f32_e32 v3, v76, v76
	v_add_f32_e32 v2, v2, v3
	v_fmamk_f32 v75, v0, 0xba000000, v75
	v_fmamk_f32 v69, v0, 0xba000000, v69
	v_add_f32_e32 v1, v1, v2
	v_fmac_f32_e32 v74, 0xba000000, v0
	v_fmac_f32_e32 v68, 0xba000000, v0
	v_mul_f32_e32 v2, v69, v69
	v_mul_f32_e32 v3, v75, v75
	v_fmac_f32_e32 v2, v68, v68
	v_fmac_f32_e32 v3, v74, v74
	v_add_f32_e32 v2, v2, v3
	v_fmamk_f32 v67, v0, 0xba000000, v67
	v_fmamk_f32 v63, v0, 0xba000000, v63
	v_add_f32_e32 v1, v1, v2
	v_fmac_f32_e32 v66, 0xba000000, v0
	v_fmac_f32_e32 v62, 0xba000000, v0
	v_mul_f32_e32 v2, v63, v63
	v_mul_f32_e32 v3, v67, v67
	v_fmac_f32_e32 v2, v62, v62
	v_fmac_f32_e32 v3, v66, v66
	v_add_f32_e32 v2, v2, v3
	v_fmamk_f32 v61, v0, 0xba000000, v61
	v_fmamk_f32 v59, v0, 0xba000000, v59
	v_add_f32_e32 v1, v1, v2
	v_fmac_f32_e32 v60, 0xba000000, v0
	v_fmac_f32_e32 v58, 0xba000000, v0
	v_mul_f32_e32 v2, v59, v59
	v_mul_f32_e32 v3, v61, v61
	v_fmac_f32_e32 v2, v58, v58
	v_fmac_f32_e32 v3, v60, v60
	v_add_f32_e32 v2, v2, v3
	v_fmamk_f32 v89, v0, 0xba000000, v89
	v_fmamk_f32 v87, v0, 0xba000000, v87
	v_add_f32_e32 v1, v1, v2
	v_fmac_f32_e32 v88, 0xba000000, v0
	v_fmac_f32_e32 v86, 0xba000000, v0
	v_mul_f32_e32 v0, v87, v87
	v_mul_f32_e32 v2, v89, v89
	v_fmac_f32_e32 v0, v86, v86
	v_fmac_f32_e32 v2, v88, v88
	v_add_f32_e32 v0, v0, v2
	v_add_f32_e32 v0, v1, v0
	s_nop 1
	v_add_f32_dpp v0, v0, v0 quad_perm:[1,0,3,2] row_mask:0xf bank_mask:0xf bound_ctrl:1
	s_nop 1
	v_add_f32_dpp v0, v0, v0 quad_perm:[2,3,0,1] row_mask:0xf bank_mask:0xf bound_ctrl:1
	s_nop 1
	v_add_f32_dpp v0, v0, v0 row_ror:4 row_mask:0xf bank_mask:0xf bound_ctrl:1
	s_nop 1
	v_add_f32_dpp v0, v0, v0 row_ror:8 row_mask:0xf bank_mask:0xf bound_ctrl:1
	v_mov_b32_e32 v1, v0
	s_nop 1
	v_permlane16_swap_b32_e32 v0, v1
	v_add_f32_e32 v0, v0, v1
	v_mov_b32_e32 v1, v0
	s_nop 1
	v_permlane32_swap_b32_e32 v0, v1
	v_add_f32_e32 v0, v0, v1
	v_fmamk_f32 v0, v0, 0x3a000000, v207
	v_rsq_f32_e32 v90, v0
	s_nop 0
	v_pk_mul_f32 v[82:83], v[90:91], v[82:83] op_sel_hi:[0,1]
	v_pk_mul_f32 v[84:85], v[90:91], v[84:85] op_sel_hi:[0,1]
	v_pk_fma_f32 v[2:3], v[84:85], v[154:155], v[190:191]
	v_pk_fma_f32 v[0:1], v[82:83], v[152:153], v[188:189]
	s_cbranch_vccz .LBB0_1338
	v_add_co_u32_e32 v6, vcc, 0x38000000, v40
	v_cvt_pk_bf16_f32 v4, v0, v1
	v_cvt_pk_bf16_f32 v5, v2, v3
	s_mov_b64 s[2:3], 0
	s_nop 0
	v_addc_co_u32_e32 v7, vcc, 0, v41, vcc
	flat_store_dwordx2 v[6:7], v[4:5] nt
